# MoE gate/up epilogue: the slot-ordered row-scale loads hoisted (8 in flight, masked with v_cndmask) instead of a conditional load + immediate wait per row group
# speedup vs baseline: 1.0313x; 1.0028x over previous
;     __device__ __forceinline__ void operator()(const f32x4 (&acc)[2][2][4][2], const Unit& u, int wr, int wc, int fr, int fq) const {
;         const int row0 = u.pm * BM + wr * 64 + fr, col0 = u.pn * HALF + wc * 32 + 8 * fq;
;         const float* cm = colmax + (size_t)u.e * 2 * ldc + u.pn * BM + wc * 32 + 8 * fq;
;         const f32x4 cg0 = *(const f32x4*)(cm), cg1 = *(const f32x4*)(cm + 4), cu0 = *(const f32x4*)(cm + HALF), cu1 = *(const f32x4*)(cm + HALF + 4);
;         const float cg[8] = {cg0[0], cg0[1], cg0[2], cg0[3], cg1[0], cg1[1], cg1[2], cg1[3]}, cu[8] = {cu0[0], cu0[1], cu0[2], cu0[3], cu1[0], cu1[1], cu1[2], cu1[3]};
;         int cume = 0, cnte = 0x7fffffff; if (rowidx) { cume = tab[8 + u.e]; cnte = tab[u.e]; }
; #pragma unroll
;         for (int ai = 0; ai < 2; ++ai)
; #pragma unroll
;             for (int m = 0; m < 4; ++m) { const int r = row0 + ai * HALF + m * 16; unsigned char* rowp = O + (size_t)r * ldc + col0;
;                 float sa; if (rowidx) { const int rl = r - cume * BM; sa = (rl < cnte) ? rowmax[u.e * ECAP + rl] : 0.f; } else sa = rowmax[r];
;                 sa *= (1.f / (127.f * 127.f));
;                 float o[8];
; #pragma unroll
;                 for (int n = 0; n < 2; ++n)
; #pragma unroll
;                     for (int j = 0; j < 4; ++j) { const float g = (float)__builtin_bit_cast(i32x4, acc[ai][0][m][n])[j] * (sa * cg[n * 4 + j]), up = (float)__builtin_bit_cast(i32x4, acc[ai][1][m][n])[j] * (sa * cu[n * 4 + j]);
;                         o[n * 4 + j] = g * __builtin_amdgcn_rcpf(1.f + __builtin_amdgcn_exp2f(-1.4426950408889634f * g)) * up; }
;                 u32x2 w; w.x = pack_fp8x4(o[0], o[1], o[2], o[3]); w.y = pack_fp8x4(o[4], o[5], o[6], o[7]);
;                 *(u32x2*)rowp = w; }
.LBB0_2297:
	s_lshl_b32 s8, s38, 8
	v_mul_hi_i32 v79, v165, s67
	v_mul_lo_u32 v78, v165, s67
	s_ashr_i32 s9, s8, 31
	v_lshl_add_u64 v[78:79], s[18:19], 0, v[78:79]
	s_lshl_b64 s[8:9], s[8:9], 2
	v_lshl_add_u64 v[78:79], v[78:79], 0, s[8:9]
	v_lshl_add_u64 v[78:79], v[78:79], 0, s[12:13]
	v_lshlrev_b32_e32 v146, 2, v165
	v_readfirstlane_b32 s8, v78
	v_readfirstlane_b32 s9, v79
	s_nop 4
	global_load_dwordx4 v[78:81], v170, s[8:9] offset:16
	global_load_dwordx4 v[86:89], v170, s[8:9]
	global_load_dwordx4 v[138:141], v170, s[8:9] offset:528
	global_load_dwordx4 v[142:145], v170, s[8:9] offset:512
	v_add_u32_e32 v146, 0, v146
	v_add_u32_e32 v146, 0x20040, v146
	ds_read2_b32 v[158:159], v146 offset1:8
	v_lshl_add_u32 v177, s74, 8, v166
	v_mov_b32_e32 v146, 0
	v_mov_b32_e32 v162, 0
	s_waitcnt lgkmcnt(0)
	v_lshlrev_b32_e32 v159, 8, v159
	v_sub_u32_e32 v156, v177, v159
	v_lshl_add_u32 v252, v165, 14, v156
	v_ashrrev_i32_e32 v253, 31, v252
	v_lshl_add_u64 v[252:253], v[252:253], 2, s[16:17]
	global_load_dword v244, v[252:253], off offset:64
	global_load_dword v245, v[252:253], off offset:128
	global_load_dword v246, v[252:253], off offset:192
	global_load_dword v247, v[252:253], off offset:512
	global_load_dword v248, v[252:253], off offset:576
	global_load_dword v249, v[252:253], off offset:640
	global_load_dword v250, v[252:253], off offset:704
	v_cmp_lt_i32_e32 vcc, v156, v158
	s_and_saveexec_b64 s[8:9], vcc
	s_cbranch_execz .LBB0_2299
	v_lshl_add_u32 v156, v165, 14, v156
	v_ashrrev_i32_e32 v157, 31, v156
	v_lshl_add_u64 v[156:157], v[156:157], 2, s[16:17]
	global_load_dword v156, v[156:157], off
	s_waitcnt vmcnt(0)
	v_mul_f32_e32 v162, 0x38820610, v156
.LBB0_2299:
	s_or_b64 exec, exec, s[8:9]
	v_cvt_f32_i32_e32 v179, v134
	v_cvt_f32_i32_e32 v178, v130
	s_waitcnt vmcnt(0)
	v_mov_b32_e32 v160, v142
	v_mov_b32_e32 v161, v86
	v_pk_mul_f32 v[180:181], v[160:161], v[162:163] op_sel_hi:[1,0]
	v_cvt_f32_i32_e32 v135, v135
	v_pk_mul_f32 v[178:179], v[180:181], v[178:179]
	v_cvt_f32_i32_e32 v134, v131
	v_mul_f32_e32 v86, 0xbfb8aa3b, v179
	v_exp_f32_e32 v142, v86
	v_mov_b32_e32 v86, v143
	v_pk_mul_f32 v[130:131], v[86:87], v[162:163] op_sel_hi:[1,0]
	v_cvt_f32_i32_e32 v137, v137
	v_pk_mul_f32 v[134:135], v[130:131], v[134:135]
	v_add_f32_e32 v131, 1.0, v142
	v_mul_f32_e32 v130, 0xbfb8aa3b, v135
	v_exp_f32_e32 v130, v130
	v_rcp_f32_e32 v131, v131
	v_cvt_f32_i32_e32 v127, v127
	v_cvt_f32_i32_e32 v129, v129
	v_add_f32_e32 v130, 1.0, v130
	v_rcp_f32_e32 v130, v130
	v_mul_f32_e32 v131, v179, v131
	v_mul_f32_e32 v182, v178, v131
	v_cvt_f32_i32_e32 v179, v136
	v_cvt_f32_i32_e32 v178, v132
	v_mul_f32_e32 v135, v135, v130
	v_mov_b32_e32 v130, v144
	v_mov_b32_e32 v131, v88
	v_pk_mul_f32 v[180:181], v[130:131], v[162:163] op_sel_hi:[1,0]
	v_cvt_f32_i32_e32 v136, v133
	v_pk_mul_f32 v[178:179], v[180:181], v[178:179]
	v_mul_f32_e32 v180, v134, v135
	v_mul_f32_e32 v88, 0xbfb8aa3b, v179
	v_exp_f32_e32 v144, v88
	v_mov_b32_e32 v88, v145
	v_pk_mul_f32 v[132:133], v[88:89], v[162:163] op_sel_hi:[1,0]
	v_cvt_f32_i32_e32 v135, v126
	v_pk_mul_f32 v[136:137], v[132:133], v[136:137]
	v_cvt_f32_i32_e32 v134, v122
	v_mul_f32_e32 v132, 0xbfb8aa3b, v137
	v_exp_f32_e32 v132, v132
	v_add_f32_e32 v133, 1.0, v144
	v_rcp_f32_e32 v181, v133
	v_mov_b32_e32 v133, v78
	v_add_f32_e32 v132, 1.0, v132
	v_rcp_f32_e32 v183, v132
	v_mov_b32_e32 v132, v138
	v_pk_mul_f32 v[144:145], v[132:133], v[162:163] op_sel_hi:[1,0]
	v_cvt_f32_i32_e32 v126, v123
	v_pk_mul_f32 v[134:135], v[144:145], v[134:135]
	v_mul_f32_e32 v122, v179, v181
	v_mul_f32_e32 v78, 0xbfb8aa3b, v135
	v_exp_f32_e32 v78, v78
	v_mul_f32_e32 v138, v178, v122
	v_mul_f32_e32 v137, v137, v183
	v_lshl_or_b32 v156, s38, 7, v168
	v_add_f32_e32 v78, 1.0, v78
	v_rcp_f32_e32 v144, v78
	v_mov_b32_e32 v78, v139
	v_pk_mul_f32 v[122:123], v[78:79], v[162:163] op_sel_hi:[1,0]
	v_mul_f32_e32 v139, v136, v137
	v_pk_mul_f32 v[126:127], v[122:123], v[126:127]
	v_mul_f32_e32 v123, v135, v144
	v_mul_f32_e32 v122, 0xbfb8aa3b, v127
	v_exp_f32_e32 v122, v122
	v_mul_f32_e32 v144, v134, v123
	v_cvt_f32_i32_e32 v135, v128
	v_cvt_f32_i32_e32 v134, v124
	v_add_f32_e32 v122, 1.0, v122
	v_rcp_f32_e32 v145, v122
	v_mov_b32_e32 v122, v140
	v_mov_b32_e32 v123, v80
	v_pk_mul_f32 v[136:137], v[122:123], v[162:163] op_sel_hi:[1,0]
	v_cvt_f32_i32_e32 v128, v125
	v_pk_mul_f32 v[134:135], v[136:137], v[134:135]
	v_mul_f32_e32 v127, v127, v145
	v_mul_f32_e32 v80, 0xbfb8aa3b, v135
	v_exp_f32_e32 v136, v80
	v_mov_b32_e32 v80, v141
	v_pk_mul_f32 v[124:125], v[80:81], v[162:163] op_sel_hi:[1,0]
	v_mul_f32_e32 v126, v126, v127
	v_pk_mul_f32 v[124:125], v[124:125], v[128:129]
	v_add_f32_e32 v129, 1.0, v136
	v_mul_f32_e32 v128, 0xbfb8aa3b, v125
	v_exp_f32_e32 v128, v128
	v_rcp_f32_e32 v129, v129
	v_med3_f32 v126, v126, s69, v171
	v_mov_b64_e32 v[142:143], s[58:59]
	v_add_f32_e32 v128, 1.0, v128
	v_rcp_f32_e32 v128, v128
	v_mul_f32_e32 v127, v135, v129
	v_med3_f32 v129, v180, s69, v171
	v_mul_f32_e32 v127, v134, v127
	v_mul_f32_e32 v125, v125, v128
	v_mul_f32_e32 v128, v124, v125
	v_med3_f32 v125, v182, s69, v171
	v_mov_b32_e32 v124, v147
	v_cvt_pk_fp8_f32 v124, v125, v129
	v_med3_f32 v129, v144, s69, v171
	v_mov_b32_e32 v125, v147
	v_cvt_pk_fp8_f32 v125, v129, v126
	v_med3_f32 v134, v138, s69, v171
	v_med3_f32 v135, v139, s69, v171
	v_med3_f32 v126, v127, s69, v171
	v_med3_f32 v127, v128, s69, v171
	v_cvt_pk_fp8_f32 v124, v134, v135 op_sel:[0,0,1]
	v_cvt_pk_fp8_f32 v125, v126, v127 op_sel:[0,0,1]
	v_ashrrev_i32_e32 v157, 31, v156
	v_mad_i64_i32 v[126:127], s[8:9], v177, s68, v[142:143]
	v_lshl_add_u64 v[126:127], v[126:127], 0, v[156:157]
	global_store_dwordx2 v[126:127], v[124:125], off
	v_or_b32_e32 v124, 16, v177
	v_sub_u32_e32 v125, v124, v159
	v_cmp_lt_i32_e32 vcc, v125, v158
	s_nop 1
	v_cndmask_b32_e32 v251, 0, v244, vcc
	v_mul_f32_e32 v146, 0x38820610, v251
;     __device__ __forceinline__ void operator()(const f32x4 (&acc)[2][2][4][2], const Unit& u, int wr, int wc, int fr, int fq) const {
;     ...
;             for (int m = 0; m < 4; ++m) { const int r = row0 + ai * HALF + m * 16; unsigned char* rowp = O + (size_t)r * ldc + col0;
;                 float sa; if (rowidx) { const int rl = r - cume * BM; sa = (rl < cnte) ? rowmax[u.e * ECAP + rl] : 0.f; } else sa = rowmax[r];
;                 sa *= (1.f / (127.f * 127.f));
;                 float o[8];
; #pragma unroll
;                 for (int n = 0; n < 2; ++n)
; #pragma unroll
;                     for (int j = 0; j < 4; ++j) { const float g = (float)__builtin_bit_cast(i32x4, acc[ai][0][m][n])[j] * (sa * cg[n * 4 + j]), up = (float)__builtin_bit_cast(i32x4, acc[ai][1][m][n])[j] * (sa * cu[n * 4 + j]);
;                         o[n * 4 + j] = g * __builtin_amdgcn_rcpf(1.f + __builtin_amdgcn_exp2f(-1.4426950408889634f * g)) * up; }
;                 u32x2 w; w.x = pack_fp8x4(o[0], o[1], o[2], o[3]); w.y = pack_fp8x4(o[4], o[5], o[6], o[7]);
;                 *(u32x2*)rowp = w; }
.LBB0_2301:
	v_cvt_f32_i32_e32 v127, v118
	v_cvt_f32_i32_e32 v126, v114
	v_pk_mul_f32 v[128:129], v[160:161], v[146:147] op_sel_hi:[1,0]
	v_cvt_f32_i32_e32 v119, v119
	v_cvt_f32_i32_e32 v118, v115
	v_pk_mul_f32 v[126:127], v[128:129], v[126:127]
	v_cvt_f32_i32_e32 v129, v120
	v_mul_f32_e32 v114, 0xbfb8aa3b, v127
	v_exp_f32_e32 v125, v114
	v_pk_mul_f32 v[114:115], v[86:87], v[146:147] op_sel_hi:[1,0]
	v_cvt_f32_i32_e32 v121, v121
	v_pk_mul_f32 v[114:115], v[114:115], v[118:119]
	v_add_f32_e32 v118, 1.0, v125
	v_rcp_f32_e32 v125, v118
	v_mul_f32_e32 v118, 0xbfb8aa3b, v115
	v_exp_f32_e32 v128, v118
	v_cvt_f32_i32_e32 v120, v117
	v_mul_f32_e32 v125, v127, v125
	v_mul_f32_e32 v125, v126, v125
	v_add_f32_e32 v127, 1.0, v128
	v_rcp_f32_e32 v127, v127
	v_cvt_f32_i32_e32 v128, v116
	v_cvt_f32_i32_e32 v111, v111
	v_cvt_f32_i32_e32 v113, v113
	v_mul_f32_e32 v115, v115, v127
	v_pk_mul_f32 v[126:127], v[130:131], v[146:147] op_sel_hi:[1,0]
	v_mov_b64_e32 v[118:119], s[58:59]
	v_pk_mul_f32 v[126:127], v[126:127], v[128:129]
	v_mul_f32_e32 v128, v114, v115
	v_mul_f32_e32 v116, 0xbfb8aa3b, v127
	v_exp_f32_e32 v116, v116
	v_pk_mul_f32 v[114:115], v[88:89], v[146:147] op_sel_hi:[1,0]
	v_add_f32_e32 v116, 1.0, v116
	v_pk_mul_f32 v[114:115], v[114:115], v[120:121]
	v_rcp_f32_e32 v129, v116
	v_mul_f32_e32 v117, 0xbfb8aa3b, v115
	v_exp_f32_e32 v120, v117
	v_cvt_f32_i32_e32 v117, v110
	v_cvt_f32_i32_e32 v116, v106
	v_add_f32_e32 v106, 1.0, v120
	v_pk_mul_f32 v[120:121], v[132:133], v[146:147] op_sel_hi:[1,0]
	v_rcp_f32_e32 v106, v106
	v_pk_mul_f32 v[116:117], v[120:121], v[116:117]
	v_mul_f32_e32 v120, v127, v129
	v_mul_f32_e32 v110, 0xbfb8aa3b, v117
	v_exp_f32_e32 v110, v110
	v_mul_f32_e32 v106, v115, v106
	v_mul_f32_e32 v121, v114, v106
	v_mul_f32_e32 v120, v126, v120
	v_add_f32_e32 v110, 1.0, v110
	v_rcp_f32_e32 v115, v110
	v_cvt_f32_i32_e32 v110, v107
	v_pk_mul_f32 v[106:107], v[78:79], v[146:147] op_sel_hi:[1,0]
	v_mul_f32_e32 v114, v117, v115
	v_pk_mul_f32 v[106:107], v[106:107], v[110:111]
	v_cvt_f32_i32_e32 v111, v112
	v_mul_f32_e32 v110, 0xbfb8aa3b, v107
	v_exp_f32_e32 v115, v110
	v_cvt_f32_i32_e32 v110, v108
	v_mul_f32_e32 v116, v116, v114
	v_cvt_f32_i32_e32 v112, v109
	v_add_f32_e32 v108, 1.0, v115
	v_pk_mul_f32 v[114:115], v[122:123], v[146:147] op_sel_hi:[1,0]
	v_rcp_f32_e32 v117, v108
	v_pk_mul_f32 v[110:111], v[114:115], v[110:111]
	v_mul_f32_e32 v107, v107, v117
	v_mul_f32_e32 v108, 0xbfb8aa3b, v111
	v_exp_f32_e32 v114, v108
	v_pk_mul_f32 v[108:109], v[80:81], v[146:147] op_sel_hi:[1,0]
	v_mul_f32_e32 v107, v106, v107
	v_pk_mul_f32 v[108:109], v[108:109], v[112:113]
	v_add_f32_e32 v113, 1.0, v114
	v_mul_f32_e32 v112, 0xbfb8aa3b, v109
	v_exp_f32_e32 v112, v112
	v_rcp_f32_e32 v113, v113
	v_add_f32_e32 v112, 1.0, v112
	v_rcp_f32_e32 v112, v112
	v_mul_f32_e32 v106, v111, v113
	v_mul_f32_e32 v110, v110, v106
	v_med3_f32 v111, v128, s69, v171
	v_mul_f32_e32 v106, v109, v112
	v_mul_f32_e32 v108, v108, v106
	v_med3_f32 v109, v125, s69, v171
	v_mov_b32_e32 v106, v147
	v_cvt_pk_fp8_f32 v106, v109, v111
	v_med3_f32 v109, v116, s69, v171
	v_med3_f32 v111, v107, s69, v171
	v_mov_b32_e32 v107, v147
	v_cvt_pk_fp8_f32 v107, v109, v111
	v_med3_f32 v112, v120, s69, v171
	v_med3_f32 v113, v121, s69, v171
	v_med3_f32 v109, v110, s69, v171
	v_med3_f32 v108, v108, s69, v171
	v_cvt_pk_fp8_f32 v106, v112, v113 op_sel:[0,0,1]
	v_cvt_pk_fp8_f32 v107, v109, v108 op_sel:[0,0,1]
	v_mad_i64_i32 v[108:109], s[8:9], v124, s68, v[118:119]
	v_lshl_add_u64 v[108:109], v[108:109], 0, v[156:157]
	global_store_dwordx2 v[108:109], v[106:107], off
	v_or_b32_e32 v107, 32, v177
	v_sub_u32_e32 v109, v107, v159
	v_cmp_lt_i32_e32 vcc, v109, v158
	v_mov_b32_e32 v106, 0
	v_mov_b32_e32 v108, 0
	s_nop 1
	v_cndmask_b32_e32 v251, 0, v245, vcc
	v_mul_f32_e32 v108, 0x38820610, v251
.LBB0_2303:
	v_cvt_f32_i32_e32 v111, v102
	v_cvt_f32_i32_e32 v110, v98
	v_pk_mul_f32 v[112:113], v[160:161], v[108:109] op_sel_hi:[1,0]
	v_cvt_f32_i32_e32 v103, v103
	v_cvt_f32_i32_e32 v102, v99
	v_pk_mul_f32 v[110:111], v[112:113], v[110:111]
	v_cvt_f32_i32_e32 v113, v104
	v_mul_f32_e32 v98, 0xbfb8aa3b, v111
	v_exp_f32_e32 v109, v98
	v_cvt_f32_i32_e32 v105, v105
	v_cvt_f32_i32_e32 v104, v101
	v_cvt_f32_i32_e32 v95, v95
	v_pk_mul_f32 v[98:99], v[86:87], v[108:109] op_sel_hi:[1,0]
	v_cvt_f32_i32_e32 v97, v97
	v_pk_mul_f32 v[98:99], v[98:99], v[102:103]
	v_add_f32_e32 v102, 1.0, v109
	v_rcp_f32_e32 v109, v102
	v_mul_f32_e32 v102, 0xbfb8aa3b, v99
	v_exp_f32_e32 v112, v102
	v_mov_b64_e32 v[102:103], s[58:59]
	v_mul_f32_e32 v109, v111, v109
	v_mul_f32_e32 v109, v110, v109
	v_add_f32_e32 v111, 1.0, v112
	v_rcp_f32_e32 v111, v111
	v_cvt_f32_i32_e32 v112, v100
	v_mul_f32_e32 v99, v99, v111
	v_pk_mul_f32 v[110:111], v[130:131], v[108:109] op_sel_hi:[1,0]
	s_nop 0
	v_pk_mul_f32 v[110:111], v[110:111], v[112:113]
	v_mul_f32_e32 v112, v98, v99
	v_mul_f32_e32 v100, 0xbfb8aa3b, v111
	v_exp_f32_e32 v100, v100
	v_pk_mul_f32 v[98:99], v[88:89], v[108:109] op_sel_hi:[1,0]
	v_add_f32_e32 v100, 1.0, v100
	v_pk_mul_f32 v[98:99], v[98:99], v[104:105]
	v_rcp_f32_e32 v113, v100
	v_mul_f32_e32 v101, 0xbfb8aa3b, v99
	v_exp_f32_e32 v104, v101
	v_cvt_f32_i32_e32 v101, v94
	v_cvt_f32_i32_e32 v100, v90
	v_add_f32_e32 v90, 1.0, v104
	v_pk_mul_f32 v[104:105], v[132:133], v[108:109] op_sel_hi:[1,0]
	v_rcp_f32_e32 v90, v90
	v_pk_mul_f32 v[100:101], v[104:105], v[100:101]
	v_mul_f32_e32 v104, v111, v113
	v_mul_f32_e32 v94, 0xbfb8aa3b, v101
	v_exp_f32_e32 v94, v94
	v_mul_f32_e32 v90, v99, v90
	v_mul_f32_e32 v105, v98, v90
	v_mul_f32_e32 v104, v110, v104
	v_add_f32_e32 v94, 1.0, v94
	v_rcp_f32_e32 v99, v94
	v_cvt_f32_i32_e32 v94, v91
;     __device__ __forceinline__ void operator()(const f32x4 (&acc)[2][2][4][2], const Unit& u, int wr, int wc, int fr, int fq) const {
;     ...
;             for (int m = 0; m < 4; ++m) { const int r = row0 + ai * HALF + m * 16; unsigned char* rowp = O + (size_t)r * ldc + col0;
;                 float sa; if (rowidx) { const int rl = r - cume * BM; sa = (rl < cnte) ? rowmax[u.e * ECAP + rl] : 0.f; } else sa = rowmax[r];
;                 sa *= (1.f / (127.f * 127.f));
;                 float o[8];
; #pragma unroll
;                 for (int n = 0; n < 2; ++n)
; #pragma unroll
;                     for (int j = 0; j < 4; ++j) { const float g = (float)__builtin_bit_cast(i32x4, acc[ai][0][m][n])[j] * (sa * cg[n * 4 + j]), up = (float)__builtin_bit_cast(i32x4, acc[ai][1][m][n])[j] * (sa * cu[n * 4 + j]);
;                         o[n * 4 + j] = g * __builtin_amdgcn_rcpf(1.f + __builtin_amdgcn_exp2f(-1.4426950408889634f * g)) * up; }
;                 u32x2 w; w.x = pack_fp8x4(o[0], o[1], o[2], o[3]); w.y = pack_fp8x4(o[4], o[5], o[6], o[7]);
;                 *(u32x2*)rowp = w; }
	v_pk_mul_f32 v[90:91], v[78:79], v[108:109] op_sel_hi:[1,0]
	v_mul_f32_e32 v98, v101, v99
	v_pk_mul_f32 v[90:91], v[90:91], v[94:95]
	v_cvt_f32_i32_e32 v95, v96
	v_mul_f32_e32 v94, 0xbfb8aa3b, v91
	v_exp_f32_e32 v99, v94
	v_cvt_f32_i32_e32 v94, v92
	v_mul_f32_e32 v100, v100, v98
	v_cvt_f32_i32_e32 v96, v93
	v_add_f32_e32 v92, 1.0, v99
	v_pk_mul_f32 v[98:99], v[122:123], v[108:109] op_sel_hi:[1,0]
	v_rcp_f32_e32 v101, v92
	v_pk_mul_f32 v[94:95], v[98:99], v[94:95]
	v_mul_f32_e32 v91, v91, v101
	v_mul_f32_e32 v92, 0xbfb8aa3b, v95
	v_exp_f32_e32 v98, v92
	v_pk_mul_f32 v[92:93], v[80:81], v[108:109] op_sel_hi:[1,0]
	v_mul_f32_e32 v91, v90, v91
	v_pk_mul_f32 v[92:93], v[92:93], v[96:97]
	v_add_f32_e32 v97, 1.0, v98
	v_mul_f32_e32 v96, 0xbfb8aa3b, v93
	v_exp_f32_e32 v96, v96
	v_rcp_f32_e32 v97, v97
	v_add_f32_e32 v96, 1.0, v96
	v_rcp_f32_e32 v96, v96
	v_mul_f32_e32 v90, v95, v97
	v_mul_f32_e32 v94, v94, v90
	v_med3_f32 v95, v112, s69, v171
	v_mul_f32_e32 v90, v93, v96
	v_mul_f32_e32 v92, v92, v90
	v_med3_f32 v93, v109, s69, v171
	v_mov_b32_e32 v90, v147
	v_cvt_pk_fp8_f32 v90, v93, v95
	v_med3_f32 v93, v100, s69, v171
	v_med3_f32 v95, v91, s69, v171
	v_mov_b32_e32 v91, v147
	v_cvt_pk_fp8_f32 v91, v93, v95
	v_med3_f32 v96, v104, s69, v171
	v_med3_f32 v97, v105, s69, v171
	v_med3_f32 v93, v94, s69, v171
	v_med3_f32 v92, v92, s69, v171
	v_cvt_pk_fp8_f32 v90, v96, v97 op_sel:[0,0,1]
	v_cvt_pk_fp8_f32 v91, v93, v92 op_sel:[0,0,1]
	v_mad_i64_i32 v[92:93], s[8:9], v107, s68, v[102:103]
	v_lshl_add_u64 v[92:93], v[92:93], 0, v[156:157]
	global_store_dwordx2 v[92:93], v[90:91], off
	v_or_b32_e32 v90, 48, v177
	v_sub_u32_e32 v91, v90, v159
	v_cmp_lt_i32_e32 vcc, v91, v158
	s_nop 1
	v_cndmask_b32_e32 v251, 0, v246, vcc
	v_mul_f32_e32 v106, 0x38820610, v251
.LBB0_2305:
	v_cvt_f32_i32_e32 v93, v82
	v_cvt_f32_i32_e32 v92, v74
	v_pk_mul_f32 v[94:95], v[160:161], v[106:107] op_sel_hi:[1,0]
	v_cvt_f32_i32_e32 v83, v83
	v_cvt_f32_i32_e32 v82, v75
	v_pk_mul_f32 v[92:93], v[94:95], v[92:93]
	v_cvt_f32_i32_e32 v95, v84
	v_mul_f32_e32 v74, 0xbfb8aa3b, v93
	v_exp_f32_e32 v91, v74
	v_pk_mul_f32 v[74:75], v[86:87], v[106:107] op_sel_hi:[1,0]
	v_cvt_f32_i32_e32 v85, v85
	v_pk_mul_f32 v[74:75], v[74:75], v[82:83]
	v_add_f32_e32 v82, 1.0, v91
	v_rcp_f32_e32 v91, v82
	v_mul_f32_e32 v82, 0xbfb8aa3b, v75
	v_exp_f32_e32 v94, v82
	v_cvt_f32_i32_e32 v84, v77
	v_mul_f32_e32 v91, v93, v91
	v_mul_f32_e32 v91, v92, v91
	v_add_f32_e32 v93, 1.0, v94
	v_rcp_f32_e32 v93, v93
	v_cvt_f32_i32_e32 v94, v76
	v_cvt_f32_i32_e32 v71, v71
	v_cvt_f32_i32_e32 v73, v73
	v_mul_f32_e32 v75, v75, v93
	v_pk_mul_f32 v[92:93], v[130:131], v[106:107] op_sel_hi:[1,0]
	v_mov_b64_e32 v[82:83], s[58:59]
	v_pk_mul_f32 v[92:93], v[92:93], v[94:95]
	v_mul_f32_e32 v94, v74, v75
	v_mul_f32_e32 v76, 0xbfb8aa3b, v93
	v_exp_f32_e32 v76, v76
	v_pk_mul_f32 v[74:75], v[88:89], v[106:107] op_sel_hi:[1,0]
	v_add_f32_e32 v76, 1.0, v76
	v_pk_mul_f32 v[74:75], v[74:75], v[84:85]
	v_rcp_f32_e32 v95, v76
	v_mul_f32_e32 v77, 0xbfb8aa3b, v75
	v_exp_f32_e32 v84, v77
	v_cvt_f32_i32_e32 v77, v70
	v_cvt_f32_i32_e32 v76, v66
	v_add_f32_e32 v66, 1.0, v84
	v_pk_mul_f32 v[84:85], v[132:133], v[106:107] op_sel_hi:[1,0]
	v_rcp_f32_e32 v66, v66
	v_pk_mul_f32 v[76:77], v[84:85], v[76:77]
	v_mul_f32_e32 v84, v93, v95
	v_mul_f32_e32 v70, 0xbfb8aa3b, v77
	v_exp_f32_e32 v70, v70
	v_mul_f32_e32 v66, v75, v66
	v_mul_f32_e32 v85, v74, v66
	v_mul_f32_e32 v84, v92, v84
	v_add_f32_e32 v70, 1.0, v70
	v_rcp_f32_e32 v75, v70
	v_cvt_f32_i32_e32 v70, v67
	v_pk_mul_f32 v[66:67], v[78:79], v[106:107] op_sel_hi:[1,0]
	v_mul_f32_e32 v74, v77, v75
	v_pk_mul_f32 v[66:67], v[66:67], v[70:71]
	v_cvt_f32_i32_e32 v71, v72
	v_mul_f32_e32 v70, 0xbfb8aa3b, v67
	v_exp_f32_e32 v75, v70
	v_cvt_f32_i32_e32 v70, v68
	v_mul_f32_e32 v76, v76, v74
	v_cvt_f32_i32_e32 v72, v69
	v_add_f32_e32 v68, 1.0, v75
	v_pk_mul_f32 v[74:75], v[122:123], v[106:107] op_sel_hi:[1,0]
	v_rcp_f32_e32 v77, v68
	v_pk_mul_f32 v[70:71], v[74:75], v[70:71]
	v_mul_f32_e32 v67, v67, v77
	v_mul_f32_e32 v68, 0xbfb8aa3b, v71
	v_exp_f32_e32 v74, v68
	v_pk_mul_f32 v[68:69], v[80:81], v[106:107] op_sel_hi:[1,0]
	v_mul_f32_e32 v67, v66, v67
	v_pk_mul_f32 v[68:69], v[68:69], v[72:73]
	v_add_f32_e32 v73, 1.0, v74
	v_mul_f32_e32 v72, 0xbfb8aa3b, v69
	v_exp_f32_e32 v72, v72
	v_rcp_f32_e32 v73, v73
	v_add_f32_e32 v72, 1.0, v72
	v_rcp_f32_e32 v72, v72
	v_mul_f32_e32 v66, v71, v73
	v_mul_f32_e32 v70, v70, v66
	v_med3_f32 v71, v94, s69, v171
	v_mul_f32_e32 v66, v69, v72
	v_mul_f32_e32 v68, v68, v66
	v_med3_f32 v69, v91, s69, v171
	v_mov_b32_e32 v66, v147
	v_cvt_pk_fp8_f32 v66, v69, v71
	v_med3_f32 v69, v76, s69, v171
	v_med3_f32 v71, v67, s69, v171
	v_mov_b32_e32 v67, v147
	v_cvt_pk_fp8_f32 v67, v69, v71
	v_med3_f32 v72, v84, s69, v171
	v_med3_f32 v73, v85, s69, v171
	v_med3_f32 v69, v70, s69, v171
	v_med3_f32 v68, v68, s69, v171
	v_cvt_pk_fp8_f32 v66, v72, v73 op_sel:[0,0,1]
	v_cvt_pk_fp8_f32 v67, v69, v68 op_sel:[0,0,1]
	v_mad_i64_i32 v[68:69], s[8:9], v90, s68, v[82:83]
	v_lshl_add_u64 v[68:69], v[68:69], 0, v[156:157]
	global_store_dwordx2 v[68:69], v[66:67], off
	v_add_u32_e32 v67, 0x80, v177
	v_sub_u32_e32 v69, v67, v159
	v_cmp_lt_i32_e32 vcc, v69, v158
	v_mov_b32_e32 v66, 0
	v_mov_b32_e32 v68, 0
	s_nop 1
	v_cndmask_b32_e32 v251, 0, v247, vcc
	v_mul_f32_e32 v68, 0x38820610, v251
;     __device__ __forceinline__ void operator()(const f32x4 (&acc)[2][2][4][2], const Unit& u, int wr, int wc, int fr, int fq) const {
;     ...
;             for (int m = 0; m < 4; ++m) { const int r = row0 + ai * HALF + m * 16; unsigned char* rowp = O + (size_t)r * ldc + col0;
;                 float sa; if (rowidx) { const int rl = r - cume * BM; sa = (rl < cnte) ? rowmax[u.e * ECAP + rl] : 0.f; } else sa = rowmax[r];
;                 sa *= (1.f / (127.f * 127.f));
;                 float o[8];
; #pragma unroll
;                 for (int n = 0; n < 2; ++n)
; #pragma unroll
;                     for (int j = 0; j < 4; ++j) { const float g = (float)__builtin_bit_cast(i32x4, acc[ai][0][m][n])[j] * (sa * cg[n * 4 + j]), up = (float)__builtin_bit_cast(i32x4, acc[ai][1][m][n])[j] * (sa * cu[n * 4 + j]);
;                         o[n * 4 + j] = g * __builtin_amdgcn_rcpf(1.f + __builtin_amdgcn_exp2f(-1.4426950408889634f * g)) * up; }
;                 u32x2 w; w.x = pack_fp8x4(o[0], o[1], o[2], o[3]); w.y = pack_fp8x4(o[4], o[5], o[6], o[7]);
;                 *(u32x2*)rowp = w; }
.LBB0_2307:
	v_cvt_f32_i32_e32 v71, v54
	v_cvt_f32_i32_e32 v70, v62
	v_pk_mul_f32 v[72:73], v[160:161], v[68:69] op_sel_hi:[1,0]
	v_cvt_f32_i32_e32 v55, v55
	v_cvt_f32_i32_e32 v54, v63
	v_pk_mul_f32 v[70:71], v[72:73], v[70:71]
	v_cvt_f32_i32_e32 v73, v56
	v_mul_f32_e32 v62, 0xbfb8aa3b, v71
	v_exp_f32_e32 v69, v62
	v_cvt_f32_i32_e32 v57, v57
	v_cvt_f32_i32_e32 v51, v51
	v_cvt_f32_i32_e32 v53, v53
	v_pk_mul_f32 v[62:63], v[86:87], v[68:69] op_sel_hi:[1,0]
	s_nop 0
	v_pk_mul_f32 v[54:55], v[62:63], v[54:55]
	v_add_f32_e32 v62, 1.0, v69
	v_rcp_f32_e32 v69, v62
	v_mul_f32_e32 v62, 0xbfb8aa3b, v55
	v_exp_f32_e32 v72, v62
	v_mov_b64_e32 v[62:63], s[58:59]
	v_mul_f32_e32 v69, v71, v69
	v_mul_f32_e32 v69, v70, v69
	v_add_f32_e32 v71, 1.0, v72
	v_rcp_f32_e32 v71, v71
	v_cvt_f32_i32_e32 v72, v64
	v_mul_f32_e32 v55, v55, v71
	v_pk_mul_f32 v[70:71], v[130:131], v[68:69] op_sel_hi:[1,0]
	s_nop 0
	v_pk_mul_f32 v[70:71], v[70:71], v[72:73]
	v_mul_f32_e32 v72, v54, v55
	v_mul_f32_e32 v56, 0xbfb8aa3b, v71
	v_exp_f32_e32 v64, v56
	v_cvt_f32_i32_e32 v56, v65
	v_pk_mul_f32 v[54:55], v[88:89], v[68:69] op_sel_hi:[1,0]
	v_add_f32_e32 v64, 1.0, v64
	v_pk_mul_f32 v[54:55], v[54:55], v[56:57]
	v_cvt_f32_i32_e32 v57, v50
	v_mul_f32_e32 v56, 0xbfb8aa3b, v55
	v_exp_f32_e32 v65, v56
	v_cvt_f32_i32_e32 v56, v58
	v_rcp_f32_e32 v73, v64
	v_add_f32_e32 v50, 1.0, v65
	v_pk_mul_f32 v[64:65], v[132:133], v[68:69] op_sel_hi:[1,0]
	v_rcp_f32_e32 v50, v50
	v_pk_mul_f32 v[56:57], v[64:65], v[56:57]
	v_mul_f32_e32 v64, v71, v73
	v_mul_f32_e32 v58, 0xbfb8aa3b, v57
	v_exp_f32_e32 v58, v58
	v_mul_f32_e32 v55, v55, v50
	v_mul_f32_e32 v64, v70, v64
	v_add_f32_e32 v50, 1.0, v58
	v_rcp_f32_e32 v58, v50
	v_cvt_f32_i32_e32 v50, v59
	v_mul_f32_e32 v59, v54, v55
	v_pk_mul_f32 v[54:55], v[78:79], v[68:69] op_sel_hi:[1,0]
	v_mul_f32_e32 v57, v57, v58
	v_pk_mul_f32 v[50:51], v[54:55], v[50:51]
	v_cvt_f32_i32_e32 v55, v52
	v_mul_f32_e32 v54, 0xbfb8aa3b, v51
	v_exp_f32_e32 v58, v54
	v_cvt_f32_i32_e32 v54, v60
	v_mul_f32_e32 v65, v56, v57
	v_pk_mul_f32 v[56:57], v[122:123], v[68:69] op_sel_hi:[1,0]
	v_add_f32_e32 v52, 1.0, v58
	v_rcp_f32_e32 v58, v52
	v_cvt_f32_i32_e32 v52, v61
	v_pk_mul_f32 v[54:55], v[56:57], v[54:55]
	v_mul_f32_e32 v51, v51, v58
	v_mul_f32_e32 v56, 0xbfb8aa3b, v55
	v_exp_f32_e32 v60, v56
	v_pk_mul_f32 v[56:57], v[80:81], v[68:69] op_sel_hi:[1,0]
	v_mul_f32_e32 v51, v50, v51
	v_pk_mul_f32 v[52:53], v[56:57], v[52:53]
	v_add_f32_e32 v57, 1.0, v60
	v_mul_f32_e32 v56, 0xbfb8aa3b, v53
	v_exp_f32_e32 v56, v56
	v_rcp_f32_e32 v57, v57
	v_add_f32_e32 v56, 1.0, v56
	v_rcp_f32_e32 v56, v56
	v_mul_f32_e32 v50, v55, v57
	v_mul_f32_e32 v54, v54, v50
	v_med3_f32 v55, v72, s69, v171
	v_mul_f32_e32 v50, v53, v56
	v_mul_f32_e32 v52, v52, v50
	v_med3_f32 v53, v69, s69, v171
	v_mov_b32_e32 v50, v147
	v_cvt_pk_fp8_f32 v50, v53, v55
	v_med3_f32 v53, v65, s69, v171
	v_med3_f32 v55, v51, s69, v171
	v_mov_b32_e32 v51, v147
	v_cvt_pk_fp8_f32 v51, v53, v55
	v_med3_f32 v56, v64, s69, v171
	v_med3_f32 v57, v59, s69, v171
	v_med3_f32 v53, v54, s69, v171
	v_med3_f32 v52, v52, s69, v171
	v_cvt_pk_fp8_f32 v50, v56, v57 op_sel:[0,0,1]
	v_cvt_pk_fp8_f32 v51, v53, v52 op_sel:[0,0,1]
	v_mad_i64_i32 v[52:53], s[8:9], v67, s68, v[62:63]
	v_lshl_add_u64 v[52:53], v[52:53], 0, v[156:157]
	global_store_dwordx2 v[52:53], v[50:51], off
	v_add_u32_e32 v50, 0x90, v177
	v_sub_u32_e32 v51, v50, v159
	v_cmp_lt_i32_e32 vcc, v51, v158
	s_nop 1
	v_cndmask_b32_e32 v251, 0, v248, vcc
	v_mul_f32_e32 v66, 0x38820610, v251
.LBB0_2309:
	v_cvt_f32_i32_e32 v53, v42
	v_cvt_f32_i32_e32 v52, v46
	v_pk_mul_f32 v[54:55], v[160:161], v[66:67] op_sel_hi:[1,0]
	v_cvt_f32_i32_e32 v43, v43
	v_cvt_f32_i32_e32 v42, v47
	v_pk_mul_f32 v[52:53], v[54:55], v[52:53]
	v_cvt_f32_i32_e32 v55, v44
	v_mul_f32_e32 v46, 0xbfb8aa3b, v53
	v_exp_f32_e32 v51, v46
	v_pk_mul_f32 v[46:47], v[86:87], v[66:67] op_sel_hi:[1,0]
	v_cvt_f32_i32_e32 v45, v45
	v_pk_mul_f32 v[42:43], v[46:47], v[42:43]
	v_add_f32_e32 v46, 1.0, v51
	v_rcp_f32_e32 v51, v46
	v_mul_f32_e32 v46, 0xbfb8aa3b, v43
	v_exp_f32_e32 v54, v46
	v_cvt_f32_i32_e32 v35, v35
	v_mul_f32_e32 v51, v53, v51
	v_mul_f32_e32 v51, v52, v51
	v_add_f32_e32 v53, 1.0, v54
	v_rcp_f32_e32 v53, v53
	v_cvt_f32_i32_e32 v54, v48
	v_cvt_f32_i32_e32 v37, v37
	v_mov_b64_e32 v[46:47], s[58:59]
	v_mul_f32_e32 v43, v43, v53
	v_pk_mul_f32 v[52:53], v[130:131], v[66:67] op_sel_hi:[1,0]
	s_nop 0
	v_pk_mul_f32 v[52:53], v[52:53], v[54:55]
	v_mul_f32_e32 v54, v42, v43
	v_mul_f32_e32 v44, 0xbfb8aa3b, v53
	v_exp_f32_e32 v48, v44
	v_cvt_f32_i32_e32 v44, v49
	v_pk_mul_f32 v[42:43], v[88:89], v[66:67] op_sel_hi:[1,0]
	v_add_f32_e32 v48, 1.0, v48
	v_pk_mul_f32 v[42:43], v[42:43], v[44:45]
	v_cvt_f32_i32_e32 v45, v34
	v_mul_f32_e32 v44, 0xbfb8aa3b, v43
	v_exp_f32_e32 v49, v44
	v_cvt_f32_i32_e32 v44, v38
	v_rcp_f32_e32 v55, v48
	v_add_f32_e32 v34, 1.0, v49
	v_pk_mul_f32 v[48:49], v[132:133], v[66:67] op_sel_hi:[1,0]
	v_rcp_f32_e32 v34, v34
	v_pk_mul_f32 v[44:45], v[48:49], v[44:45]
	v_mul_f32_e32 v48, v53, v55
	v_mul_f32_e32 v38, 0xbfb8aa3b, v45
	v_exp_f32_e32 v38, v38
	v_mul_f32_e32 v43, v43, v34
	v_mul_f32_e32 v49, v42, v43
	v_mul_f32_e32 v48, v52, v48
	v_add_f32_e32 v34, 1.0, v38
	v_rcp_f32_e32 v38, v34
	v_cvt_f32_i32_e32 v34, v39
	v_mul_f32_e32 v42, v45, v38
	v_pk_mul_f32 v[38:39], v[78:79], v[66:67] op_sel_hi:[1,0]
	v_mul_f32_e32 v44, v44, v42
	v_pk_mul_f32 v[34:35], v[38:39], v[34:35]
	v_cvt_f32_i32_e32 v39, v36
	v_mul_f32_e32 v38, 0xbfb8aa3b, v35
	v_exp_f32_e32 v43, v38
	v_cvt_f32_i32_e32 v38, v40
	v_add_f32_e32 v36, 1.0, v43
	v_rcp_f32_e32 v45, v36
	v_pk_mul_f32 v[42:43], v[122:123], v[66:67] op_sel_hi:[1,0]
	v_cvt_f32_i32_e32 v36, v41
	v_pk_mul_f32 v[38:39], v[42:43], v[38:39]
	v_mul_f32_e32 v35, v35, v45
	v_mul_f32_e32 v40, 0xbfb8aa3b, v39
	v_exp_f32_e32 v42, v40
	v_pk_mul_f32 v[40:41], v[80:81], v[66:67] op_sel_hi:[1,0]
	v_mul_f32_e32 v35, v34, v35
	v_pk_mul_f32 v[36:37], v[40:41], v[36:37]
	v_add_f32_e32 v41, 1.0, v42
	v_mul_f32_e32 v40, 0xbfb8aa3b, v37
	v_exp_f32_e32 v40, v40
	v_rcp_f32_e32 v41, v41
	v_add_f32_e32 v40, 1.0, v40
	v_rcp_f32_e32 v40, v40
	v_mul_f32_e32 v34, v39, v41
	v_mul_f32_e32 v38, v38, v34
	v_med3_f32 v39, v54, s69, v171
	v_mul_f32_e32 v34, v37, v40
	v_mul_f32_e32 v36, v36, v34
	v_med3_f32 v37, v51, s69, v171
	v_mov_b32_e32 v34, v147
	v_cvt_pk_fp8_f32 v34, v37, v39
	v_med3_f32 v37, v44, s69, v171
	v_med3_f32 v39, v35, s69, v171
	v_mov_b32_e32 v35, v147
	v_cvt_pk_fp8_f32 v35, v37, v39
	v_med3_f32 v40, v48, s69, v171
	v_med3_f32 v41, v49, s69, v171
	v_med3_f32 v37, v38, s69, v171
	v_med3_f32 v36, v36, s69, v171
	v_cvt_pk_fp8_f32 v34, v40, v41 op_sel:[0,0,1]
	v_cvt_pk_fp8_f32 v35, v37, v36 op_sel:[0,0,1]
	v_mad_i64_i32 v[36:37], s[8:9], v50, s68, v[46:47]
	v_lshl_add_u64 v[36:37], v[36:37], 0, v[156:157]
	global_store_dwordx2 v[36:37], v[34:35], off
	v_add_u32_e32 v35, 0xa0, v177
	v_sub_u32_e32 v37, v35, v159
	v_cmp_lt_i32_e32 vcc, v37, v158
	v_mov_b32_e32 v34, 0
	v_mov_b32_e32 v36, 0
	s_nop 1
	v_cndmask_b32_e32 v251, 0, v249, vcc
	v_mul_f32_e32 v36, 0x38820610, v251
;     __device__ __forceinline__ void operator()(const f32x4 (&acc)[2][2][4][2], const Unit& u, int wr, int wc, int fr, int fq) const {
;     ...
;             for (int m = 0; m < 4; ++m) { const int r = row0 + ai * HALF + m * 16; unsigned char* rowp = O + (size_t)r * ldc + col0;
;                 float sa; if (rowidx) { const int rl = r - cume * BM; sa = (rl < cnte) ? rowmax[u.e * ECAP + rl] : 0.f; } else sa = rowmax[r];
;                 sa *= (1.f / (127.f * 127.f));
;                 float o[8];
; #pragma unroll
;                 for (int n = 0; n < 2; ++n)
; #pragma unroll
;                     for (int j = 0; j < 4; ++j) { const float g = (float)__builtin_bit_cast(i32x4, acc[ai][0][m][n])[j] * (sa * cg[n * 4 + j]), up = (float)__builtin_bit_cast(i32x4, acc[ai][1][m][n])[j] * (sa * cu[n * 4 + j]);
;                         o[n * 4 + j] = g * __builtin_amdgcn_rcpf(1.f + __builtin_amdgcn_exp2f(-1.4426950408889634f * g)) * up; }
;                 u32x2 w; w.x = pack_fp8x4(o[0], o[1], o[2], o[3]); w.y = pack_fp8x4(o[4], o[5], o[6], o[7]);
;                 *(u32x2*)rowp = w; }
.LBB0_2311:
	v_cvt_f32_i32_e32 v39, v26
	v_cvt_f32_i32_e32 v38, v30
	v_pk_mul_f32 v[40:41], v[160:161], v[36:37] op_sel_hi:[1,0]
	v_cvt_f32_i32_e32 v27, v27
	v_cvt_f32_i32_e32 v26, v31
	v_pk_mul_f32 v[38:39], v[40:41], v[38:39]
	v_cvt_f32_i32_e32 v41, v28
	v_mul_f32_e32 v30, 0xbfb8aa3b, v39
	v_exp_f32_e32 v37, v30
	v_cvt_f32_i32_e32 v29, v29
	v_cvt_f32_i32_e32 v19, v19
	v_cvt_f32_i32_e32 v21, v21
	v_pk_mul_f32 v[30:31], v[86:87], v[36:37] op_sel_hi:[1,0]
	s_nop 0
	v_pk_mul_f32 v[26:27], v[30:31], v[26:27]
	v_add_f32_e32 v30, 1.0, v37
	v_rcp_f32_e32 v37, v30
	v_mul_f32_e32 v30, 0xbfb8aa3b, v27
	v_exp_f32_e32 v40, v30
	v_mov_b64_e32 v[30:31], s[58:59]
	v_mul_f32_e32 v37, v39, v37
	v_mul_f32_e32 v37, v38, v37
	v_add_f32_e32 v39, 1.0, v40
	v_rcp_f32_e32 v39, v39
	v_cvt_f32_i32_e32 v40, v32
	v_mul_f32_e32 v27, v27, v39
	v_pk_mul_f32 v[38:39], v[130:131], v[36:37] op_sel_hi:[1,0]
	s_nop 0
	v_pk_mul_f32 v[38:39], v[38:39], v[40:41]
	v_mul_f32_e32 v40, v26, v27
	v_mul_f32_e32 v28, 0xbfb8aa3b, v39
	v_exp_f32_e32 v32, v28
	v_cvt_f32_i32_e32 v28, v33
	v_pk_mul_f32 v[26:27], v[88:89], v[36:37] op_sel_hi:[1,0]
	v_add_f32_e32 v32, 1.0, v32
	v_pk_mul_f32 v[26:27], v[26:27], v[28:29]
	v_cvt_f32_i32_e32 v29, v18
	v_mul_f32_e32 v28, 0xbfb8aa3b, v27
	v_exp_f32_e32 v33, v28
	v_cvt_f32_i32_e32 v28, v22
	v_rcp_f32_e32 v41, v32
	v_add_f32_e32 v18, 1.0, v33
	v_pk_mul_f32 v[32:33], v[132:133], v[36:37] op_sel_hi:[1,0]
	v_rcp_f32_e32 v18, v18
	v_pk_mul_f32 v[28:29], v[32:33], v[28:29]
	v_mul_f32_e32 v32, v39, v41
	v_mul_f32_e32 v22, 0xbfb8aa3b, v29
	v_exp_f32_e32 v22, v22
	v_mul_f32_e32 v27, v27, v18
	v_mul_f32_e32 v33, v26, v27
	v_mul_f32_e32 v32, v38, v32
	v_add_f32_e32 v18, 1.0, v22
	v_rcp_f32_e32 v22, v18
	v_cvt_f32_i32_e32 v18, v23
	v_mul_f32_e32 v26, v29, v22
	v_pk_mul_f32 v[22:23], v[78:79], v[36:37] op_sel_hi:[1,0]
	v_mul_f32_e32 v28, v28, v26
	v_pk_mul_f32 v[18:19], v[22:23], v[18:19]
	v_cvt_f32_i32_e32 v23, v20
	v_mul_f32_e32 v22, 0xbfb8aa3b, v19
	v_exp_f32_e32 v27, v22
	v_cvt_f32_i32_e32 v22, v24
	v_add_f32_e32 v20, 1.0, v27
	v_rcp_f32_e32 v29, v20
	v_pk_mul_f32 v[26:27], v[122:123], v[36:37] op_sel_hi:[1,0]
	v_cvt_f32_i32_e32 v20, v25
	v_pk_mul_f32 v[22:23], v[26:27], v[22:23]
	v_mul_f32_e32 v19, v19, v29
	v_mul_f32_e32 v24, 0xbfb8aa3b, v23
	v_exp_f32_e32 v26, v24
	v_pk_mul_f32 v[24:25], v[80:81], v[36:37] op_sel_hi:[1,0]
	v_mul_f32_e32 v19, v18, v19
	v_pk_mul_f32 v[20:21], v[24:25], v[20:21]
	v_add_f32_e32 v25, 1.0, v26
	v_mul_f32_e32 v24, 0xbfb8aa3b, v21
	v_exp_f32_e32 v24, v24
	v_rcp_f32_e32 v25, v25
	v_add_f32_e32 v24, 1.0, v24
	v_rcp_f32_e32 v24, v24
	v_mul_f32_e32 v18, v23, v25
	v_mul_f32_e32 v22, v22, v18
	v_med3_f32 v23, v40, s69, v171
	v_mul_f32_e32 v18, v21, v24
	v_mul_f32_e32 v20, v20, v18
	v_med3_f32 v21, v37, s69, v171
	v_mov_b32_e32 v18, v147
	v_cvt_pk_fp8_f32 v18, v21, v23
	v_med3_f32 v21, v28, s69, v171
	v_med3_f32 v23, v19, s69, v171
	v_mov_b32_e32 v19, v147
	v_cvt_pk_fp8_f32 v19, v21, v23
	v_med3_f32 v24, v32, s69, v171
	v_med3_f32 v25, v33, s69, v171
	v_med3_f32 v21, v22, s69, v171
	v_med3_f32 v20, v20, s69, v171
	v_cvt_pk_fp8_f32 v18, v24, v25 op_sel:[0,0,1]
	v_cvt_pk_fp8_f32 v19, v21, v20 op_sel:[0,0,1]
	v_mad_i64_i32 v[20:21], s[8:9], v35, s68, v[30:31]
	v_lshl_add_u64 v[20:21], v[20:21], 0, v[156:157]
	global_store_dwordx2 v[20:21], v[18:19], off
	v_add_u32_e32 v18, 0xb0, v177
	v_sub_u32_e32 v19, v18, v159
	v_cmp_lt_i32_e32 vcc, v19, v158
	s_nop 1
	v_cndmask_b32_e32 v251, 0, v250, vcc
	v_mul_f32_e32 v34, 0x38820610, v251
.LBB0_2313:
	v_cvt_f32_i32_e32 v21, v10
	v_cvt_f32_i32_e32 v20, v14
	v_pk_mul_f32 v[22:23], v[160:161], v[34:35] op_sel_hi:[1,0]
	v_cvt_f32_i32_e32 v11, v11
	v_cvt_f32_i32_e32 v10, v15
	v_pk_mul_f32 v[20:21], v[22:23], v[20:21]
	v_cvt_f32_i32_e32 v23, v12
	v_mul_f32_e32 v14, 0xbfb8aa3b, v21
	v_exp_f32_e32 v19, v14
	v_pk_mul_f32 v[14:15], v[86:87], v[34:35] op_sel_hi:[1,0]
	v_cvt_f32_i32_e32 v13, v13
	v_pk_mul_f32 v[10:11], v[14:15], v[10:11]
	v_add_f32_e32 v14, 1.0, v19
	v_rcp_f32_e32 v19, v14
	v_mul_f32_e32 v14, 0xbfb8aa3b, v11
	v_exp_f32_e32 v22, v14
	v_cvt_f32_i32_e32 v3, v3
	v_mul_f32_e32 v19, v21, v19
	v_mul_f32_e32 v19, v20, v19
	v_add_f32_e32 v21, 1.0, v22
	v_rcp_f32_e32 v21, v21
	v_cvt_f32_i32_e32 v22, v16
	v_cvt_f32_i32_e32 v5, v5
	v_mov_b64_e32 v[14:15], s[58:59]
	v_mul_f32_e32 v11, v11, v21
	v_pk_mul_f32 v[20:21], v[130:131], v[34:35] op_sel_hi:[1,0]
	s_and_b64 vcc, exec, s[6:7]
	v_pk_mul_f32 v[20:21], v[20:21], v[22:23]
	v_mul_f32_e32 v22, v10, v11
	v_mul_f32_e32 v12, 0xbfb8aa3b, v21
	v_exp_f32_e32 v16, v12
	v_cvt_f32_i32_e32 v12, v17
	v_pk_mul_f32 v[10:11], v[88:89], v[34:35] op_sel_hi:[1,0]
	s_mov_b64 s[6:7], -1
	v_add_f32_e32 v16, 1.0, v16
	v_pk_mul_f32 v[10:11], v[10:11], v[12:13]
	v_cvt_f32_i32_e32 v13, v2
	v_mul_f32_e32 v12, 0xbfb8aa3b, v11
	v_exp_f32_e32 v17, v12
	v_cvt_f32_i32_e32 v12, v6
	v_rcp_f32_e32 v23, v16
	v_add_f32_e32 v2, 1.0, v17
	v_pk_mul_f32 v[16:17], v[132:133], v[34:35] op_sel_hi:[1,0]
	v_rcp_f32_e32 v2, v2
	v_pk_mul_f32 v[12:13], v[16:17], v[12:13]
	v_mul_f32_e32 v16, v21, v23
	v_mul_f32_e32 v6, 0xbfb8aa3b, v13
	v_exp_f32_e32 v6, v6
	v_mul_f32_e32 v11, v11, v2
	v_mul_f32_e32 v17, v10, v11
	v_mul_f32_e32 v16, v20, v16
	v_add_f32_e32 v2, 1.0, v6
	v_rcp_f32_e32 v6, v2
	v_cvt_f32_i32_e32 v2, v7
	v_mul_f32_e32 v10, v13, v6
	v_pk_mul_f32 v[6:7], v[78:79], v[34:35] op_sel_hi:[1,0]
	v_mul_f32_e32 v12, v12, v10
	v_pk_mul_f32 v[2:3], v[6:7], v[2:3]
	v_cvt_f32_i32_e32 v7, v4
	v_mul_f32_e32 v6, 0xbfb8aa3b, v3
	v_exp_f32_e32 v11, v6
	v_cvt_f32_i32_e32 v6, v8
	v_add_f32_e32 v4, 1.0, v11
	v_rcp_f32_e32 v13, v4
	v_pk_mul_f32 v[10:11], v[122:123], v[34:35] op_sel_hi:[1,0]
	v_cvt_f32_i32_e32 v4, v9
	v_pk_mul_f32 v[6:7], v[10:11], v[6:7]
	v_mul_f32_e32 v3, v3, v13
	v_mul_f32_e32 v8, 0xbfb8aa3b, v7
	v_exp_f32_e32 v10, v8
	v_pk_mul_f32 v[8:9], v[80:81], v[34:35] op_sel_hi:[1,0]
	v_mul_f32_e32 v3, v2, v3
	v_pk_mul_f32 v[4:5], v[8:9], v[4:5]
	v_add_f32_e32 v9, 1.0, v10
	v_mul_f32_e32 v8, 0xbfb8aa3b, v5
	v_exp_f32_e32 v8, v8
	v_rcp_f32_e32 v9, v9
	v_add_f32_e32 v8, 1.0, v8
	v_rcp_f32_e32 v8, v8
	v_mul_f32_e32 v2, v7, v9
	v_mul_f32_e32 v6, v6, v2
	v_med3_f32 v7, v22, s69, v171
	v_mul_f32_e32 v2, v5, v8
	v_mul_f32_e32 v4, v4, v2
	v_med3_f32 v5, v19, s69, v171
	v_mov_b32_e32 v2, v147
	v_cvt_pk_fp8_f32 v2, v5, v7
	v_med3_f32 v5, v12, s69, v171
	v_med3_f32 v7, v3, s69, v171
	v_mov_b32_e32 v3, v147
	v_cvt_pk_fp8_f32 v3, v5, v7
	v_med3_f32 v8, v16, s69, v171
	v_med3_f32 v9, v17, s69, v171
	v_med3_f32 v5, v6, s69, v171
	v_med3_f32 v4, v4, s69, v171
	v_cvt_pk_fp8_f32 v2, v8, v9 op_sel:[0,0,1]
	v_cvt_pk_fp8_f32 v3, v5, v4 op_sel:[0,0,1]
	v_mad_i64_i32 v[4:5], s[8:9], v18, s68, v[14:15]
	v_lshl_add_u64 v[4:5], v[4:5], 0, v[156:157]
	global_store_dwordx2 v[4:5], v[2:3], off
	s_cbranch_vccnz .LBB0_2274
	s_andn2_b64 vcc, exec, s[14:15]
	s_cbranch_vccnz .LBB0_2273
	s_barrier
	s_branch .LBB0_2273
